# v64 + non-temporal hint on the write-once streams: moe2's y row stores (read once by norm2) and pconv's bf16 p stores
# speedup vs baseline: 1.0085x; 1.0008x over previous
; #define LAS __attribute__((address_space(3)))
; __device__ __forceinline__ u32x4 pack8(f32x4 a, f32x4 b) { u32x4 w; w.x = pk2(a[0], a[1]); w.y = pk2(a[2], a[3]); w.z = pk2(b[0], b[1]); w.w = pk2(b[2], b[3]); return w; }
;     __device__ __forceinline__ void operator()(const f32x4 (&acc)[2][2][4][2], const Unit& u, int ui, int wr, int wc, int fr, int fq, LAS unsigned char* lds) const {
; #pragma unroll
;         for (int ai = 0; ai < 2; ++ai)
; #pragma unroll
;             for (int m = 0; m < 4; ++m) {
;                 const int row = u.pm * 256 + ai * 128 + wr * 64 + m * 16 + fr;
; #pragma unroll
;                 for (int bj = 0; bj < 2; ++bj) { const int c = u.pn * 256 + bj * 128 + wc * 32 + fq * 8;
;                     *(u32x4*)(O + (size_t)row * ldc + c) = pack8(acc[ai][bj][m][0], acc[ai][bj][m][1]); }
;             }
;     }
.LBB0_1231:
	v_mov_b32_e32 v135, v188
	s_lshl_b32 s35, s47, 8
	s_add_i32 s35, s35, s40
	v_and_or_b32 v136, v135, 15, s35
	s_lshl_b32 s35, s48, 8
	v_lshrrev_b32_e32 v135, 1, v135
	v_and_or_b32 v135, v135, 24, s35
	v_or_b32_e32 v138, s41, v135
	v_ashrrev_i32_e32 v137, 31, v136
	v_cvt_pk_bf16_f32 v114, v114, v115
	v_cvt_pk_bf16_f32 v115, v116, v117
	v_cvt_pk_bf16_f32 v116, v118, v119
	v_lshlrev_b64 v[118:119], 11, v[136:137]
	v_ashrrev_i32_e32 v139, 31, v138
	v_cvt_pk_bf16_f32 v117, v120, v121
	v_lshl_add_u64 v[118:119], s[18:19], 0, v[118:119]
	v_lshlrev_b64 v[120:121], 1, v[138:139]
	v_lshl_add_u64 v[118:119], v[118:119], 0, v[120:121]
	flat_store_dwordx4 v[118:119], v[114:117] nt
	v_cvt_pk_bf16_f32 v98, v98, v99
	v_cvt_pk_bf16_f32 v99, v100, v101
	v_cvt_pk_bf16_f32 v114, v122, v123
	v_cvt_pk_bf16_f32 v115, v124, v125
	v_cvt_pk_bf16_f32 v116, v126, v127
	v_cvt_pk_bf16_f32 v117, v128, v129
	flat_store_dwordx4 v[118:119], v[114:117] offset:256 nt
	v_cvt_pk_bf16_f32 v100, v102, v103
	v_cvt_pk_bf16_f32 v101, v104, v105
	v_or_b32_e32 v114, 16, v136
	v_ashrrev_i32_e32 v115, 31, v114
	v_lshlrev_b64 v[102:103], 11, v[114:115]
	v_lshl_add_u64 v[102:103], s[18:19], 0, v[102:103]
	v_lshl_add_u64 v[102:103], v[102:103], 0, v[120:121]
	flat_store_dwordx4 v[102:103], v[98:101] nt
	v_cvt_pk_bf16_f32 v66, v66, v67
	v_cvt_pk_bf16_f32 v67, v68, v69
	v_cvt_pk_bf16_f32 v98, v106, v107
	v_cvt_pk_bf16_f32 v99, v108, v109
	v_cvt_pk_bf16_f32 v100, v110, v111
	v_cvt_pk_bf16_f32 v101, v112, v113
	flat_store_dwordx4 v[102:103], v[98:101] offset:256 nt
	v_cvt_pk_bf16_f32 v68, v70, v71
	v_cvt_pk_bf16_f32 v69, v72, v73
	v_or_b32_e32 v98, 32, v136
	v_ashrrev_i32_e32 v99, 31, v98
	v_lshlrev_b64 v[70:71], 11, v[98:99]
	v_lshl_add_u64 v[70:71], s[18:19], 0, v[70:71]
	v_lshl_add_u64 v[70:71], v[70:71], 0, v[120:121]
	flat_store_dwordx4 v[70:71], v[66:69] nt
	v_cvt_pk_bf16_f32 v34, v34, v35
	v_cvt_pk_bf16_f32 v35, v36, v37
	v_cvt_pk_bf16_f32 v66, v74, v75
	v_cvt_pk_bf16_f32 v67, v76, v77
	v_cvt_pk_bf16_f32 v68, v78, v79
	v_cvt_pk_bf16_f32 v69, v80, v81
	flat_store_dwordx4 v[70:71], v[66:69] offset:256 nt
	v_cvt_pk_bf16_f32 v36, v38, v39
	v_cvt_pk_bf16_f32 v37, v40, v41
	v_or_b32_e32 v66, 48, v136
	v_ashrrev_i32_e32 v67, 31, v66
	v_lshlrev_b64 v[38:39], 11, v[66:67]
	v_lshl_add_u64 v[38:39], s[18:19], 0, v[38:39]
	v_lshl_add_u64 v[38:39], v[38:39], 0, v[120:121]
	flat_store_dwordx4 v[38:39], v[34:37] nt
	v_cvt_pk_bf16_f32 v18, v18, v19
	v_cvt_pk_bf16_f32 v19, v20, v21
	v_cvt_pk_bf16_f32 v34, v42, v43
	v_cvt_pk_bf16_f32 v35, v44, v45
	v_cvt_pk_bf16_f32 v36, v46, v47
	v_cvt_pk_bf16_f32 v37, v48, v49
	flat_store_dwordx4 v[38:39], v[34:37] offset:256 nt
	v_add_u32_e32 v38, 0x80, v136
	v_ashrrev_i32_e32 v39, 31, v38
	v_lshlrev_b64 v[38:39], 11, v[38:39]
	v_lshl_add_u64 v[38:39], s[18:19], 0, v[38:39]
	v_cvt_pk_bf16_f32 v34, v82, v83
	v_cvt_pk_bf16_f32 v35, v84, v85
	v_cvt_pk_bf16_f32 v36, v86, v87
	v_cvt_pk_bf16_f32 v37, v88, v89
	v_lshl_add_u64 v[38:39], v[38:39], 0, v[120:121]
	flat_store_dwordx4 v[38:39], v[34:37] nt
	v_cvt_pk_bf16_f32 v20, v22, v23
	v_cvt_pk_bf16_f32 v21, v24, v25
	v_cvt_pk_bf16_f32 v34, v90, v91
	v_cvt_pk_bf16_f32 v35, v92, v93
	v_cvt_pk_bf16_f32 v36, v94, v95
	v_cvt_pk_bf16_f32 v37, v96, v97
	flat_store_dwordx4 v[38:39], v[34:37] offset:256 nt
	v_add_u32_e32 v38, 0x90, v136
	v_ashrrev_i32_e32 v39, 31, v38
	v_lshlrev_b64 v[38:39], 11, v[38:39]
	v_lshl_add_u64 v[38:39], s[18:19], 0, v[38:39]
	v_cvt_pk_bf16_f32 v34, v50, v51
	v_cvt_pk_bf16_f32 v35, v52, v53
	v_cvt_pk_bf16_f32 v36, v54, v55
	v_cvt_pk_bf16_f32 v37, v56, v57
	v_lshl_add_u64 v[38:39], v[38:39], 0, v[120:121]
	flat_store_dwordx4 v[38:39], v[34:37] nt
	v_cvt_pk_bf16_f32 v2, v2, v3
	v_cvt_pk_bf16_f32 v3, v4, v5
	v_cvt_pk_bf16_f32 v34, v58, v59
	v_cvt_pk_bf16_f32 v35, v60, v61
	v_cvt_pk_bf16_f32 v36, v62, v63
	v_cvt_pk_bf16_f32 v37, v64, v65
	flat_store_dwordx4 v[38:39], v[34:37] offset:256 nt
	v_cvt_pk_bf16_f32 v4, v6, v7
	v_cvt_pk_bf16_f32 v5, v8, v9
	v_add_u32_e32 v34, 0xa0, v136
	v_ashrrev_i32_e32 v35, 31, v34
	v_lshlrev_b64 v[22:23], 11, v[34:35]
	v_lshl_add_u64 v[22:23], s[18:19], 0, v[22:23]
	v_lshl_add_u64 v[22:23], v[22:23], 0, v[120:121]
	flat_store_dwordx4 v[22:23], v[18:21] nt
	s_mov_b64 s[36:37], -1
	v_readfirstlane_b32 s35, v0
	v_cvt_pk_bf16_f32 v18, v26, v27
	v_cvt_pk_bf16_f32 v19, v28, v29
	v_cvt_pk_bf16_f32 v20, v30, v31
	v_cvt_pk_bf16_f32 v21, v32, v33
	flat_store_dwordx4 v[22:23], v[18:21] offset:256 nt
	s_and_b64 vcc, exec, s[10:11]
	v_readfirstlane_b32 s10, v0
	v_add_u32_e32 v18, 0xb0, v136
	v_ashrrev_i32_e32 v19, 31, v18
	v_lshlrev_b64 v[6:7], 11, v[18:19]
	v_lshl_add_u64 v[6:7], s[18:19], 0, v[6:7]
	v_lshl_add_u64 v[6:7], v[6:7], 0, v[120:121]
	flat_store_dwordx4 v[6:7], v[2:5] nt
	v_readlane_b32 s58, v255, 17
	v_readlane_b32 s55, v255, 18
	v_cvt_pk_bf16_f32 v2, v10, v11
	v_cvt_pk_bf16_f32 v3, v12, v13
	v_cvt_pk_bf16_f32 v4, v14, v15
	v_cvt_pk_bf16_f32 v5, v16, v17
	v_mov_b64_e32 v[248:249], v[250:251]
	v_mov_b64_e32 v[238:239], 0x47f
	v_mov_b32_e32 v234, 0x30000
	v_mov_b32_e32 v235, v252
	v_mov_b32_e32 v251, 0x260
	v_mov_b32_e32 v236, 0x358637bd
	flat_store_dwordx4 v[6:7], v[2:5] offset:256 nt
	s_cbranch_vccnz .LBB0_1224
	ds_read_b128 v[2:5], v132
	s_andn2_b64 vcc, exec, s[16:17]
	s_cbranch_vccnz .LBB0_1223
	s_barrier
	s_branch .LBB0_1223

; __device__ __forceinline__ u32x4 pack8(f32x4 a, f32x4 b) { u32x4 w; w.x = pk2(a[0], a[1]); w.y = pk2(a[2], a[3]); w.z = pk2(b[0], b[1]); w.w = pk2(b[2], b[3]); return w; }
; template <class Tp> __device__ __forceinline__ Tp* wsp(const Frame& F, size_t off) { return (Tp*)(F.ws + off); }
; __device__ __forceinline__ void phase_pconv(Frame& F, int l) {
;     const Params& P = *F.P; bf16_t* PB = wsp<bf16_t>(F, WS_PB); const float* pl = P.in[1] + (size_t)l * T * DPLE;
;     for (int i = F.bx * NTHREADS + F.tid; i < T * DPLE / 16; i += F.G * NTHREADS) {
;         const f32x4* pp = (const f32x4*)(pl + (size_t)i * 16); const f32x4 a = pp[0], b2 = pp[1], c2 = pp[2], d2 = pp[3];
;         u32x4* dst = (u32x4*)(PB + (size_t)i * 16); dst[0] = pack8(a, b2); dst[1] = pack8(c2, d2); }
; }
.LBB0_1469:
	s_or_b64 exec, exec, s[44:45]
	s_cmp_eq_u32 s62, 3
	s_waitcnt lgkmcnt(0)
	s_barrier
	s_cbranch_scc1 .LBB0_1474
	v_readlane_b32 s2, v253, 3
	s_nop 1
	v_add_u32_e32 v2, s2, v188
	s_mov_b32 s2, 0x80000
	v_cmp_gt_i32_e32 vcc, s2, v2
	s_and_saveexec_b64 s[10:11], vcc
	v_readlane_b32 s16, v255, 28
	v_readlane_b32 s18, v255, 30
	v_readlane_b32 s6, v255, 26
	v_readlane_b32 s17, v255, 29
	v_readlane_b32 s19, v255, 31
	v_readlane_b32 s7, v255, 27
	s_cbranch_execz .LBB0_1473
	v_ashrrev_i32_e32 v3, 31, v2
	v_lshlrev_b64 v[6:7], 5, v[2:3]
	v_lshl_add_u64 v[6:7], s[74:75], 0, v[6:7]
	s_mov_b64 s[2:3], 0x2ac00010
	v_readlane_b32 s14, v254, 51
	v_lshlrev_b64 v[4:5], 6, v[2:3]
	v_lshl_add_u64 v[6:7], v[6:7], 0, s[2:3]
	s_mov_b64 s[12:13], 0
	v_readlane_b32 s15, v254, 52
	s_cmp_lg_u32 s6, 0x20000
	s_cbranch_scc1 .LBB0_1472
	v_lshl_add_u64 v[20:21], s[14:15], 0, v[4:5]
	global_load_dwordx4 v[24:27], v[20:21], off nt
	global_load_dwordx4 v[28:31], v[20:21], off offset:16 nt
	global_load_dwordx4 v[32:35], v[20:21], off offset:32 nt
	global_load_dwordx4 v[36:39], v[20:21], off offset:48 nt
	s_add_u32 s14, s14, s16
	s_addc_u32 s15, s15, s17
	v_lshl_add_u64 v[20:21], s[14:15], 0, v[4:5]
	global_load_dwordx4 v[40:43], v[20:21], off nt
	global_load_dwordx4 v[44:47], v[20:21], off offset:16 nt
	global_load_dwordx4 v[48:51], v[20:21], off offset:32 nt
	global_load_dwordx4 v[52:55], v[20:21], off offset:48 nt
	s_add_u32 s14, s14, s16
	s_addc_u32 s15, s15, s17
	v_lshl_add_u64 v[20:21], s[14:15], 0, v[4:5]
	global_load_dwordx4 v[56:59], v[20:21], off nt
	global_load_dwordx4 v[60:63], v[20:21], off offset:16 nt
	global_load_dwordx4 v[64:67], v[20:21], off offset:32 nt
	global_load_dwordx4 v[68:71], v[20:21], off offset:48 nt
	s_add_u32 s14, s14, s16
	s_addc_u32 s15, s15, s17
	v_lshl_add_u64 v[20:21], s[14:15], 0, v[4:5]
	global_load_dwordx4 v[72:75], v[20:21], off nt
	global_load_dwordx4 v[76:79], v[20:21], off offset:16 nt
	global_load_dwordx4 v[80:83], v[20:21], off offset:32 nt
	global_load_dwordx4 v[84:87], v[20:21], off offset:48 nt
	s_add_u32 s14, s14, s16
	s_addc_u32 s15, s15, s17
	s_waitcnt vmcnt(12)
	v_cvt_pk_bf16_f32 v8, v24, v25
	v_cvt_pk_bf16_f32 v9, v26, v27
	v_cvt_pk_bf16_f32 v10, v28, v29
	v_cvt_pk_bf16_f32 v11, v30, v31
	v_cvt_pk_bf16_f32 v12, v32, v33
	v_cvt_pk_bf16_f32 v13, v34, v35
	v_cvt_pk_bf16_f32 v14, v36, v37
	v_cvt_pk_bf16_f32 v15, v38, v39
	global_store_dwordx4 v[6:7], v[8:11], off offset:-16 nt
	global_store_dwordx4 v[6:7], v[12:15], off nt
	s_nop 1
	v_lshl_add_u64 v[6:7], v[6:7], 0, s[18:19]
	s_waitcnt vmcnt(10)
	v_cvt_pk_bf16_f32 v8, v40, v41
	v_cvt_pk_bf16_f32 v9, v42, v43
	v_cvt_pk_bf16_f32 v10, v44, v45
	v_cvt_pk_bf16_f32 v11, v46, v47
	v_cvt_pk_bf16_f32 v12, v48, v49
	v_cvt_pk_bf16_f32 v13, v50, v51
	v_cvt_pk_bf16_f32 v14, v52, v53
	v_cvt_pk_bf16_f32 v15, v54, v55
	global_store_dwordx4 v[6:7], v[8:11], off offset:-16 nt
	global_store_dwordx4 v[6:7], v[12:15], off nt
	s_nop 1
	v_lshl_add_u64 v[6:7], v[6:7], 0, s[18:19]
	s_waitcnt vmcnt(8)
	v_cvt_pk_bf16_f32 v8, v56, v57
	v_cvt_pk_bf16_f32 v9, v58, v59
	v_cvt_pk_bf16_f32 v10, v60, v61
	v_cvt_pk_bf16_f32 v11, v62, v63
	v_cvt_pk_bf16_f32 v12, v64, v65
	v_cvt_pk_bf16_f32 v13, v66, v67
	v_cvt_pk_bf16_f32 v14, v68, v69
	v_cvt_pk_bf16_f32 v15, v70, v71
	global_store_dwordx4 v[6:7], v[8:11], off offset:-16 nt
	global_store_dwordx4 v[6:7], v[12:15], off nt
	s_nop 1
	v_lshl_add_u64 v[6:7], v[6:7], 0, s[18:19]
	s_waitcnt vmcnt(6)
	v_cvt_pk_bf16_f32 v8, v72, v73
	v_cvt_pk_bf16_f32 v9, v74, v75
	v_cvt_pk_bf16_f32 v10, v76, v77
	v_cvt_pk_bf16_f32 v11, v78, v79
	v_cvt_pk_bf16_f32 v12, v80, v81
	v_cvt_pk_bf16_f32 v13, v82, v83
	v_cvt_pk_bf16_f32 v14, v84, v85
	v_cvt_pk_bf16_f32 v15, v86, v87
	global_store_dwordx4 v[6:7], v[8:11], off offset:-16 nt
	global_store_dwordx4 v[6:7], v[12:15], off nt
	s_nop 1
	v_lshl_add_u64 v[6:7], v[6:7], 0, s[18:19]
	s_branch .LBB0_1473
.LBB0_1472:
	s_nop 1
	v_lshl_add_u64 v[20:21], s[14:15], 0, v[4:5]
	global_load_dwordx4 v[8:11], v[20:21], off offset:48 nt
	global_load_dwordx4 v[12:15], v[20:21], off offset:32 nt
	global_load_dwordx4 v[16:19], v[20:21], off offset:16 nt
	s_nop 0
	global_load_dwordx4 v[20:23], v[20:21], off nt
	v_add_u32_e32 v2, s6, v2
	s_add_u32 s14, s14, s16
	s_mov_b32 s2, 0x7ffff
	s_addc_u32 s15, s15, s17
	s_waitcnt vmcnt(0)
	v_cvt_pk_bf16_f32 v12, v12, v13
	v_cvt_pk_bf16_f32 v13, v14, v15
	v_cvt_pk_bf16_f32 v20, v20, v21
	v_cvt_pk_bf16_f32 v21, v22, v23
	v_cvt_pk_bf16_f32 v22, v16, v17
	v_add_co_u32_e32 v16, vcc, -16, v6
	v_cvt_pk_bf16_f32 v14, v8, v9
	s_nop 0
	v_addc_co_u32_e32 v17, vcc, -1, v7, vcc
	v_cvt_pk_bf16_f32 v15, v10, v11
	v_cmp_lt_i32_e32 vcc, s2, v2
	v_cvt_pk_bf16_f32 v23, v18, v19
	flat_store_dwordx4 v[6:7], v[12:15] nt
	v_lshl_add_u64 v[6:7], v[6:7], 0, s[18:19]
	s_or_b64 s[12:13], vcc, s[12:13]
	flat_store_dwordx4 v[16:17], v[20:23] nt
	s_andn2_b64 exec, exec, s[12:13]
	s_cbranch_execnz .LBB0_1472
